# baseline (speedup 1.0000x reference)
.LBB3_5:
.LBB3_6:
	v_add_u32_e32 v167, s18, v109
	v_add_u32_e32 v166, v167, v110
	ds_read_b128 v[158:161], v166 offset:8192
	ds_read_b128 v[162:165], v166 offset:12288
	s_nop 0
	v_exp_f32_e32 v120, v66
	v_exp_f32_e32 v121, v67
	v_exp_f32_e32 v122, v68
	v_exp_f32_e32 v123, v69
	v_exp_f32_e32 v124, v70
	v_exp_f32_e32 v125, v71
	v_exp_f32_e32 v126, v72
	v_exp_f32_e32 v127, v73
	v_exp_f32_e32 v128, v74
	v_exp_f32_e32 v129, v75
	v_exp_f32_e32 v130, v76
	v_exp_f32_e32 v131, v77
	v_exp_f32_e32 v132, v78
	v_exp_f32_e32 v133, v79
	v_exp_f32_e32 v134, v80
	v_exp_f32_e32 v135, v81
	v_exp_f32_e32 v136, v50
	v_exp_f32_e32 v137, v51
	v_exp_f32_e32 v138, v52
	v_exp_f32_e32 v139, v53
	v_exp_f32_e32 v140, v54
	v_exp_f32_e32 v141, v55
	v_exp_f32_e32 v142, v56
	v_exp_f32_e32 v143, v57
	v_exp_f32_e32 v150, v58
	v_exp_f32_e32 v151, v59
	v_exp_f32_e32 v152, v60
	v_exp_f32_e32 v153, v61
	v_exp_f32_e32 v154, v62
	v_exp_f32_e32 v155, v63
	v_exp_f32_e32 v156, v64
	v_exp_f32_e32 v157, v65
	v_add_f32_e32 v144, v120, v121
	v_add_f32_e32 v166, v122, v123
	v_add_f32_e32 v144, v144, v124
	v_add_f32_e32 v166, v166, v125
	v_add_f32_e32 v144, v144, v126
	v_add_f32_e32 v166, v166, v127
	v_add_f32_e32 v144, v144, v128
	v_add_f32_e32 v166, v166, v129
	v_add_f32_e32 v144, v144, v130
	v_add_f32_e32 v166, v166, v131
	v_add_f32_e32 v144, v144, v132
	v_add_f32_e32 v166, v166, v133
	v_add_f32_e32 v144, v144, v134
	v_add_f32_e32 v166, v166, v135
	v_add_f32_e32 v144, v144, v136
	v_add_f32_e32 v166, v166, v137
	v_add_f32_e32 v144, v144, v138
	v_add_f32_e32 v166, v166, v139
	v_add_f32_e32 v144, v144, v140
	v_add_f32_e32 v166, v166, v141
	v_add_f32_e32 v144, v144, v142
	v_add_f32_e32 v166, v166, v143
	v_add_f32_e32 v144, v144, v150
	v_add_f32_e32 v166, v166, v151
	v_add_f32_e32 v144, v144, v152
	v_add_f32_e32 v166, v166, v153
	v_add_f32_e32 v144, v144, v154
	v_add_f32_e32 v166, v166, v155
	v_add_f32_e32 v144, v144, v156
	v_add_f32_e32 v166, v166, v157
	v_add_f32_e32 v144, v144, v166
	s_nop 0
	v_cmp_lt_f32_e32 vcc, s8, v144
	v_cmp_gt_f32_e64 s[46:47], s45, v144
	s_or_b64 vcc, vcc, s[46:47]
	s_cbranch_vccnz .Lattn_slow
	s_mov_b32 s44, 0
	s_mov_b32 s45, 0xbf800000
	v_add_u32_e32 v166, v167, v112
	ds_read_b128 v[50:53], v166 offset:8192
	ds_read_b128 v[54:57], v166 offset:12288
	s_add_i32 s9, s9, 1
	s_add_i32 s6, s23, 1
	s_cmp_lg_u32 s23, 2
	s_cselect_b32 s23, s6, 0
	v_cvt_pk_f16_f32 v66, v120, v121
	v_cvt_pk_f16_f32 v67, v122, v123
	v_cvt_pk_f16_f32 v68, v124, v125
	v_cvt_pk_f16_f32 v69, v126, v127
	v_cvt_pk_f16_f32 v70, v128, v129
	v_cvt_pk_f16_f32 v71, v130, v131
	v_cvt_pk_f16_f32 v72, v132, v133
	v_cvt_pk_f16_f32 v73, v134, v135
	v_add_u32_e32 v166, v167, v111
	v_add_u32_e32 v167, v167, v113
	s_waitcnt lgkmcnt(2)
	s_setprio 1
	v_mfma_f32_32x32x16_f16 v[18:33], v[158:161], v[66:69], v[18:33]
	v_mfma_f32_32x32x16_f16 v[2:17], v[162:165], v[66:69], v[2:17]
	ds_read_b128 v[58:61], v166 offset:8192
	ds_read_b128 v[62:65], v166 offset:12288
	v_cvt_pk_f16_f32 v74, v136, v137
	v_cvt_pk_f16_f32 v75, v138, v139
	v_cvt_pk_f16_f32 v76, v140, v141
	v_cvt_pk_f16_f32 v77, v142, v143
	s_waitcnt lgkmcnt(2)
	v_mfma_f32_32x32x16_f16 v[18:33], v[50:53], v[70:73], v[18:33]
	v_mfma_f32_32x32x16_f16 v[2:17], v[54:57], v[70:73], v[2:17]
	ds_read_b128 v[120:123], v167 offset:8192
	ds_read_b128 v[124:127], v167 offset:12288
	v_cvt_pk_f16_f32 v78, v150, v151
	v_cvt_pk_f16_f32 v79, v152, v153
	v_cvt_pk_f16_f32 v80, v154, v155
	v_cvt_pk_f16_f32 v81, v156, v157
	v_add_f32_e32 v114, v114, v144
	s_waitcnt lgkmcnt(2)
	v_mfma_f32_32x32x16_f16 v[18:33], v[58:61], v[74:77], v[18:33]
	v_mfma_f32_32x32x16_f16 v[2:17], v[62:65], v[74:77], v[2:17]
	s_waitcnt lgkmcnt(0)
	v_mfma_f32_32x32x16_f16 v[18:33], v[120:123], v[78:81], v[18:33]
	v_mfma_f32_32x32x16_f16 v[2:17], v[124:127], v[78:81], v[2:17]
	s_setprio 0
	s_cmp_eq_u32 s9, 16
	s_cbranch_scc0 .LBB3_1
	s_branch .LBB3_8

.LBB3_8:
	s_waitcnt vmcnt(0)
	v_mov_b32_e32 v35, v114
	v_mov_b32_e32 v40, v114
	s_nop 1
	v_permlane32_swap_b32_e32 v35, v40
	v_add_f32_e32 v35, v35, v40
	v_cmp_gt_u32_e32 vcc, 32, v99
	s_and_saveexec_b64 s[4:5], vcc
	s_cbranch_execz .LBB3_11
	s_mul_i32 s6, s20, 24
	s_add_u32 s6, s6, s12
	s_addc_u32 s7, 0, s13
	s_lshl_b64 s[6:7], s[6:7], 14
	s_add_u32 s6, s0, s6
	s_addc_u32 s7, s1, s7
	s_lshl_b64 s[0:1], s[2:3], 3
	s_add_u32 s0, s6, s0
	v_xor_b32_e32 v34, 0x80000000, v34
	s_addc_u32 s1, s7, s1
	v_lshlrev_b32_e32 v36, 3, v98
	global_store_dwordx2 v36, v[34:35], s[0:1]
.LBB3_11:
	s_or_b64 exec, exec, s[4:5]
	s_mul_hi_i32 s0, s12, 0x2aaaaaab
	s_lshr_b32 s3, s0, 31
	s_ashr_i32 s4, s0, 1
	v_div_scale_f32 v34, s[0:1], v35, v35, 1.0
	v_rcp_f32_e32 v36, v34
	s_add_i32 s0, s4, s3
	s_mul_i32 s3, s21, 0x1200
	s_movk_i32 s4, 0x90
	v_fma_f32 v37, -v34, v36, 1.0
	v_fmac_f32_e32 v36, v37, v36
	v_div_scale_f32 v37, vcc, 1.0, v35, 1.0
	v_mul_f32_e32 v38, v37, v36
	v_fma_f32 v39, -v34, v38, v37
	v_fmac_f32_e32 v38, v39, v36
	v_fma_f32 v34, -v34, v38, v37
	v_div_fmas_f32 v34, v34, v36, v38
	v_div_fixup_f32 v34, v34, v35, 1.0
	v_mov_b32_e32 v35, s3
	v_mad_u32_u24 v35, v98, s4, v35
	v_or_b32_e32 v35, v35, v108
	v_fma_mixlo_f16 v36, v34, v18, 0
	v_mov_b32_e32 v18, v19
	v_mov_b32_e32 v19, v20
	v_pk_mul_f32 v[18:19], v[34:35], v[18:19] op_sel_hi:[0,1]
	v_cvt_pk_f16_f32 v20, v18, v19
	v_mov_b32_e32 v18, v3
	v_mov_b32_e32 v19, v4
	v_pk_mul_f32 v[18:19], v[34:35], v[18:19] op_sel_hi:[0,1]
	v_fma_mixlo_f16 v37, v34, v2, 0
	v_cvt_pk_f16_f32 v18, v18, v19
	v_fma_mixlo_f16 v5, v34, v5, 0
	v_pack_b32_f16 v4, v37, v18
	v_alignbit_b32 v5, v5, v18, 16
	v_mov_b32_e32 v18, v23
	v_mov_b32_e32 v19, v24
	v_fma_mixlo_f16 v3, v34, v21, 0
	v_pk_mul_f32 v[18:19], v[34:35], v[18:19] op_sel_hi:[0,1]
	v_pack_b32_f16 v2, v36, v20
	v_alignbit_b32 v3, v3, v20, 16
	v_fma_mixlo_f16 v20, v34, v22, 0
	v_cvt_pk_f16_f32 v22, v18, v19
	v_mov_b32_e32 v18, v7
	v_mov_b32_e32 v19, v8
	v_pk_mul_f32 v[18:19], v[34:35], v[18:19] op_sel_hi:[0,1]
	v_fma_mixlo_f16 v7, v34, v25, 0
	v_fma_mixlo_f16 v21, v34, v6, 0
	v_pack_b32_f16 v6, v20, v22
	v_cvt_pk_f16_f32 v18, v18, v19
	v_alignbit_b32 v7, v7, v22, 16
	v_fma_mixlo_f16 v9, v34, v9, 0
	s_waitcnt vmcnt(0)
	s_barrier
	v_pack_b32_f16 v8, v21, v18
	v_alignbit_b32 v9, v9, v18, 16
	ds_write2_b64 v35, v[2:3], v[6:7] offset1:2
	ds_write2_b64 v35, v[4:5], v[8:9] offset0:8 offset1:10
	v_mov_b32_e32 v2, v27
	v_mov_b32_e32 v3, v28
	v_pk_mul_f32 v[2:3], v[34:35], v[2:3] op_sel_hi:[0,1]
	v_fma_mixlo_f16 v4, v34, v26, 0
	v_cvt_pk_f16_f32 v3, v2, v3
	v_pack_b32_f16 v2, v4, v3
	v_mov_b32_e32 v4, v11
	v_mov_b32_e32 v5, v12
	v_pk_mul_f32 v[4:5], v[34:35], v[4:5] op_sel_hi:[0,1]
	v_fma_mixlo_f16 v6, v34, v10, 0
	v_cvt_pk_f16_f32 v5, v4, v5
	v_pack_b32_f16 v4, v6, v5
	v_fma_mixlo_f16 v6, v34, v29, 0
	s_mul_i32 s1, s0, 12
	v_alignbit_b32 v3, v6, v3, 16
	v_fma_mixlo_f16 v6, v34, v13, 0
	s_sub_i32 s1, s12, s1
	v_alignbit_b32 v5, v6, v5, 16
	v_mov_b32_e32 v6, v31
	v_mov_b32_e32 v7, v32
	s_mul_i32 s20, s20, 0x600000
	v_pk_mul_f32 v[6:7], v[34:35], v[6:7] op_sel_hi:[0,1]
	s_add_u32 s5, s10, s20
	v_fma_mixlo_f16 v8, v34, v30, 0
	v_cvt_pk_f16_f32 v7, v6, v7
	s_addc_u32 s6, s11, 0
	s_lshl_b32 s0, s0, 11
	v_pack_b32_f16 v6, v8, v7
	v_mov_b32_e32 v8, v15
	v_mov_b32_e32 v9, v16
	s_add_i32 s0, s2, s0
	v_pk_mul_f32 v[8:9], v[34:35], v[8:9] op_sel_hi:[0,1]
	s_mul_hi_i32 s2, s0, 0x600
	s_mulk_i32 s0, 0x600
	v_fma_mixlo_f16 v10, v34, v14, 0
	v_cvt_pk_f16_f32 v9, v8, v9
	s_add_u32 s5, s5, s0
	v_pack_b32_f16 v8, v10, v9
	v_fma_mixlo_f16 v10, v34, v33, 0
	s_addc_u32 s2, s6, s2
	s_lshl_b32 s0, s1, 6
	v_and_b32_e32 v0, 7, v0
	v_alignbit_b32 v7, v10, v7, 16
	v_fma_mixlo_f16 v10, v34, v17, 0
	s_ashr_i32 s1, s0, 31
	v_alignbit_b32 v9, v10, v9, 16
	ds_write2_b64 v35, v[2:3], v[6:7] offset0:4 offset1:6
	ds_write2_b64 v35, v[4:5], v[8:9] offset0:12 offset1:14
	s_lshl_b64 s[0:1], s[0:1], 1
	v_lshlrev_b32_e32 v6, 4, v0
	s_add_u32 s0, s5, s0
	v_or_b32_e32 v0, s3, v6
	s_addc_u32 s1, s2, s1
	v_mov_b32_e32 v7, 0
	v_mad_u32_u24 v12, v1, s4, v0
	v_mul_u32_u24_e32 v0, 0x300, v1
	s_waitcnt lgkmcnt(0)
	v_lshl_add_u64 v[8:9], s[0:1], 0, v[6:7]
	v_lshlrev_b32_e32 v6, 1, v0
	ds_read_b128 v[2:5], v12
	v_lshl_add_u64 v[10:11], v[8:9], 0, v[6:7]
	ds_read_b128 v[6:9], v12 offset:1152
	s_movk_i32 s0, 0x3000
	v_add_co_u32_e32 v0, vcc, s0, v10
	s_waitcnt lgkmcnt(1)
	global_store_dwordx4 v[10:11], v[2:5], off nt
	v_addc_co_u32_e32 v1, vcc, 0, v11, vcc
	s_waitcnt lgkmcnt(0)
	global_store_dwordx4 v[0:1], v[6:9], off nt
	ds_read_b128 v[0:3], v12 offset:2304
	ds_read_b128 v[4:7], v12 offset:3456
	v_add_co_u32_e32 v8, vcc, 0x6000, v10
	s_nop 1
	v_addc_co_u32_e32 v9, vcc, 0, v11, vcc
	s_waitcnt lgkmcnt(1)
	global_store_dwordx4 v[8:9], v[0:3], off nt
	s_nop 1
	v_add_co_u32_e32 v0, vcc, 0x9000, v10
	s_nop 1
	v_addc_co_u32_e32 v1, vcc, 0, v11, vcc
	s_waitcnt lgkmcnt(0)
	global_store_dwordx4 v[0:1], v[4:7], off nt
	s_endpgm
	.section	.rodata,"a",@progbits
	.p2align	6, 0x0
